# grid barrier: acquire invalidate (buffer_inv sc1) issued at arrival instead of after release
# speedup vs baseline: 1.0057x; 1.0057x over previous
; __device__ __forceinline__ unsigned xb_ld(unsigned* p)              { return __hip_atomic_load(p, __ATOMIC_RELAXED, __HIP_MEMORY_SCOPE_AGENT); }
; __device__ __forceinline__ unsigned xb_add(unsigned* p, unsigned v) { return __hip_atomic_fetch_add(p, v, __ATOMIC_RELAXED, __HIP_MEMORY_SCOPE_AGENT); }
; #define XB_SPIN(cond, bar) do { unsigned _sp = 0; while (cond) { __builtin_amdgcn_s_sleep(1); \
;     if ((++_sp & 255u) == 0u) { if (xb_ld(&(bar)[XB_TMO])) break; if (_sp > XB_SPIN_CAP) { atomicAdd(&(bar)[XB_TMO], 1u); break; } } } } while (0)
; __device__ __forceinline__ void xcd_barrier(const XcdBarrier& b) {
;     ...
;         unsigned nloc = b.st[0], nx = b.st[1];
;         if (nloc == 0u) { xcd_barrier_complete(bar, b.x, nloc, nx); b.st[0] = nloc; b.st[1] = nx; }
;         const unsigned old = xb_add(&bar[XB_XSUB(b.x)], 1u);
;         const unsigned gen = old / nloc;
;         if (old + 1u == (gen + 1u) * nloc) {
;             __builtin_amdgcn_fence(__ATOMIC_RELEASE, "agent");
;             asm volatile("s_waitcnt vmcnt(0)" ::: "memory");
;             const unsigned og = xb_add(&bar[XB_TOP], 1u);
;             const unsigned tg = og / nx;
;             if (og + 1u == (tg + 1u) * nx) xb_add(&bar[XB_TOPGEN], 1u);
;             else XB_SPIN(xb_ld(&bar[XB_TOPGEN]) == tg, bar);
;             __builtin_amdgcn_fence(__ATOMIC_ACQUIRE, "agent");
;             xb_add(&bar[XB_XGEN(b.x)], 1u);
;             asm volatile("s_waitcnt vmcnt(0)" ::: "memory");
;         } else {
;             XB_SPIN(xb_ld(&bar[XB_XGEN(b.x)]) == gen, bar);
.LBB0_111:
	s_lshl_b32 s4, s33, 8
	s_add_u32 s4, s84, s4
	s_addc_u32 s5, s85, 0
	v_mov_b32_e32 v2, 0x1000
	v_mov_b32_e32 v4, 1
	global_atomic_add v4, v2, v4, s[4:5] offset:1024 sc0
	buffer_inv sc1
	v_cvt_f32_u32_e32 v2, v3
	v_sub_u32_e32 v5, 0, v3
	v_rcp_iflag_f32_e32 v2, v2
	s_nop 0
	v_mul_f32_e32 v2, 0x4f7ffffe, v2
	v_cvt_u32_f32_e32 v2, v2
	v_mul_lo_u32 v5, v5, v2
	v_mul_hi_u32 v5, v2, v5
	v_add_u32_e32 v2, v2, v5
	s_waitcnt vmcnt(1)
	v_mul_hi_u32 v2, v4, v2
	v_mul_lo_u32 v5, v2, v3
	v_sub_u32_e32 v5, v4, v5
	v_add_u32_e32 v6, 1, v2
	v_cmp_ge_u32_e32 vcc, v5, v3
	v_add_u32_e32 v4, 1, v4
	s_nop 0
	v_cndmask_b32_e32 v2, v2, v6, vcc
	v_sub_u32_e32 v6, v5, v3
	v_cndmask_b32_e32 v5, v5, v6, vcc
	v_add_u32_e32 v6, 1, v2
	v_cmp_ge_u32_e32 vcc, v5, v3
	s_nop 1
	v_cndmask_b32_e32 v2, v2, v6, vcc
	v_mul_lo_u32 v5, v3, v2
	v_add_u32_e32 v3, v5, v3
	v_cmp_ne_u32_e32 vcc, v4, v3
	s_and_saveexec_b64 s[6:7], vcc
	s_xor_b64 s[6:7], exec, s[6:7]
	s_cbranch_execz .LBB0_125
	s_waitcnt lgkmcnt(0)
	v_mov_b32_e32 v1, 0x2000
	global_load_dword v1, v1, s[4:5] offset:1024 sc1
	s_add_u32 s10, s4, 0x2400
	s_addc_u32 s11, s5, 0
	s_waitcnt vmcnt(0)
	v_cmp_eq_u32_e32 vcc, v1, v2
	s_and_saveexec_b64 s[8:9], vcc
	s_cbranch_execz .LBB0_124
	s_mov_b32 s16, 1
	s_mov_b64 s[12:13], 0
	v_mov_b32_e32 v1, 0
	s_branch .LBB0_115

; __device__ __forceinline__ unsigned xb_ld(unsigned* p)              { return __hip_atomic_load(p, __ATOMIC_RELAXED, __HIP_MEMORY_SCOPE_AGENT); }
; #define XB_SPIN(cond, bar) do { unsigned _sp = 0; while (cond) { __builtin_amdgcn_s_sleep(1); \
;     if ((++_sp & 255u) == 0u) { if (xb_ld(&(bar)[XB_TMO])) break; if (_sp > XB_SPIN_CAP) { atomicAdd(&(bar)[XB_TMO], 1u); break; } } } } while (0)
; __device__ __forceinline__ void xcd_barrier(const XcdBarrier& b) {
;     ...
;             XB_SPIN(xb_ld(&bar[XB_XGEN(b.x)]) == gen, bar);
;             __builtin_amdgcn_fence(__ATOMIC_ACQUIRE, "agent");
;             asm volatile("s_waitcnt vmcnt(0)" ::: "memory");
.LBB0_124:
	s_or_b64 exec, exec, s[8:9]
	s_waitcnt vmcnt(0)
	s_waitcnt vmcnt(0)

; __device__ __forceinline__ unsigned xb_add(unsigned* p, unsigned v) { return __hip_atomic_fetch_add(p, v, __ATOMIC_RELAXED, __HIP_MEMORY_SCOPE_AGENT); }
; __device__ __forceinline__ void xcd_barrier(const XcdBarrier& b) {
;     ...
;             __builtin_amdgcn_fence(__ATOMIC_ACQUIRE, "agent");
;             xb_add(&bar[XB_XGEN(b.x)], 1u);
;             asm volatile("s_waitcnt vmcnt(0)" ::: "memory");
.LBB0_142:
	s_or_b64 exec, exec, s[6:7]
	v_mov_b32_e32 v1, 0x2000
	v_mov_b32_e32 v2, 1
	s_waitcnt vmcnt(0)
	global_atomic_add v1, v2, s[4:5] offset:1024
	s_waitcnt vmcnt(0)

; __device__ __forceinline__ unsigned xb_ld(unsigned* p)              { return __hip_atomic_load(p, __ATOMIC_RELAXED, __HIP_MEMORY_SCOPE_AGENT); }
; __device__ __forceinline__ unsigned xb_add(unsigned* p, unsigned v) { return __hip_atomic_fetch_add(p, v, __ATOMIC_RELAXED, __HIP_MEMORY_SCOPE_AGENT); }
; #define XB_SPIN(cond, bar) do { unsigned _sp = 0; while (cond) { __builtin_amdgcn_s_sleep(1); \
;     if ((++_sp & 255u) == 0u) { if (xb_ld(&(bar)[XB_TMO])) break; if (_sp > XB_SPIN_CAP) { atomicAdd(&(bar)[XB_TMO], 1u); break; } } } } while (0)
; __device__ __forceinline__ void xcd_barrier(const XcdBarrier& b) {
;     ...
;         unsigned nloc = b.st[0], nx = b.st[1];
;         if (nloc == 0u) { xcd_barrier_complete(bar, b.x, nloc, nx); b.st[0] = nloc; b.st[1] = nx; }
;         const unsigned old = xb_add(&bar[XB_XSUB(b.x)], 1u);
;         const unsigned gen = old / nloc;
;         if (old + 1u == (gen + 1u) * nloc) {
;             __builtin_amdgcn_fence(__ATOMIC_RELEASE, "agent");
;             asm volatile("s_waitcnt vmcnt(0)" ::: "memory");
;             const unsigned og = xb_add(&bar[XB_TOP], 1u);
;             const unsigned tg = og / nx;
;             if (og + 1u == (tg + 1u) * nx) xb_add(&bar[XB_TOPGEN], 1u);
;             else XB_SPIN(xb_ld(&bar[XB_TOPGEN]) == tg, bar);
;             __builtin_amdgcn_fence(__ATOMIC_ACQUIRE, "agent");
;             xb_add(&bar[XB_XGEN(b.x)], 1u);
;             asm volatile("s_waitcnt vmcnt(0)" ::: "memory");
;         } else {
;             XB_SPIN(xb_ld(&bar[XB_XGEN(b.x)]) == gen, bar);
.LBB0_169:
	s_lshl_b32 s2, s33, 8
	s_add_u32 s2, s84, s2
	s_addc_u32 s3, s85, 0
	v_mov_b32_e32 v2, 0x1000
	v_mov_b32_e32 v4, 1
	global_atomic_add v4, v2, v4, s[2:3] offset:1024 sc0
	buffer_inv sc1
	v_cvt_f32_u32_e32 v2, v3
	v_sub_u32_e32 v5, 0, v3
	v_rcp_iflag_f32_e32 v2, v2
	s_nop 0
	v_mul_f32_e32 v2, 0x4f7ffffe, v2
	v_cvt_u32_f32_e32 v2, v2
	v_mul_lo_u32 v5, v5, v2
	v_mul_hi_u32 v5, v2, v5
	v_add_u32_e32 v2, v2, v5
	s_waitcnt vmcnt(1)
	v_mul_hi_u32 v2, v4, v2
	v_mul_lo_u32 v5, v2, v3
	v_sub_u32_e32 v5, v4, v5
	v_add_u32_e32 v6, 1, v2
	v_cmp_ge_u32_e32 vcc, v5, v3
	v_add_u32_e32 v4, 1, v4
	s_nop 0
	v_cndmask_b32_e32 v2, v2, v6, vcc
	v_sub_u32_e32 v6, v5, v3
	v_cndmask_b32_e32 v5, v5, v6, vcc
	v_add_u32_e32 v6, 1, v2
	v_cmp_ge_u32_e32 vcc, v5, v3
	s_nop 1
	v_cndmask_b32_e32 v2, v2, v6, vcc
	v_mul_lo_u32 v5, v3, v2
	v_add_u32_e32 v3, v5, v3
	v_cmp_ne_u32_e32 vcc, v4, v3
	s_and_saveexec_b64 s[4:5], vcc
	s_xor_b64 s[4:5], exec, s[4:5]
	s_cbranch_execz .LBB0_183
	s_waitcnt lgkmcnt(0)
	v_mov_b32_e32 v1, 0x2000
	global_load_dword v1, v1, s[2:3] offset:1024 sc1
	s_add_u32 s8, s2, 0x2400
	s_addc_u32 s9, s3, 0
	s_waitcnt vmcnt(0)
	v_cmp_eq_u32_e32 vcc, v1, v2
	s_and_saveexec_b64 s[6:7], vcc
	s_cbranch_execz .LBB0_182
	s_mov_b32 s16, 1
	s_mov_b64 s[10:11], 0
	v_mov_b32_e32 v1, 0
	s_branch .LBB0_173

; __device__ __forceinline__ unsigned xb_ld(unsigned* p)              { return __hip_atomic_load(p, __ATOMIC_RELAXED, __HIP_MEMORY_SCOPE_AGENT); }
; #define XB_SPIN(cond, bar) do { unsigned _sp = 0; while (cond) { __builtin_amdgcn_s_sleep(1); \
;     if ((++_sp & 255u) == 0u) { if (xb_ld(&(bar)[XB_TMO])) break; if (_sp > XB_SPIN_CAP) { atomicAdd(&(bar)[XB_TMO], 1u); break; } } } } while (0)
; __device__ __forceinline__ void xcd_barrier(const XcdBarrier& b) {
;     ...
;             XB_SPIN(xb_ld(&bar[XB_XGEN(b.x)]) == gen, bar);
;             __builtin_amdgcn_fence(__ATOMIC_ACQUIRE, "agent");
;             asm volatile("s_waitcnt vmcnt(0)" ::: "memory");
.LBB0_182:
	s_or_b64 exec, exec, s[6:7]
	s_waitcnt vmcnt(0)
	s_waitcnt vmcnt(0)

; __device__ __forceinline__ unsigned xb_add(unsigned* p, unsigned v) { return __hip_atomic_fetch_add(p, v, __ATOMIC_RELAXED, __HIP_MEMORY_SCOPE_AGENT); }
; __device__ __forceinline__ void xcd_barrier(const XcdBarrier& b) {
;     ...
;             __builtin_amdgcn_fence(__ATOMIC_ACQUIRE, "agent");
;             xb_add(&bar[XB_XGEN(b.x)], 1u);
;             asm volatile("s_waitcnt vmcnt(0)" ::: "memory");
.LBB0_200:
	s_or_b64 exec, exec, s[4:5]
	v_mov_b32_e32 v1, 0x2000
	v_mov_b32_e32 v2, 1
	s_waitcnt vmcnt(0)
	global_atomic_add v1, v2, s[2:3] offset:1024
	s_waitcnt vmcnt(0)

; __device__ __forceinline__ unsigned xb_add(unsigned* p, unsigned v) { return __hip_atomic_fetch_add(p, v, __ATOMIC_RELAXED, __HIP_MEMORY_SCOPE_AGENT); }
; __device__ __forceinline__ void xcd_barrier(const XcdBarrier& b) {
;     ...
;             __builtin_amdgcn_fence(__ATOMIC_ACQUIRE, "agent");
;             xb_add(&bar[XB_XGEN(b.x)], 1u);
;             asm volatile("s_waitcnt vmcnt(0)" ::: "memory");
.LBB0_203:
	s_or_b64 exec, exec, s[2:3]
	v_readlane_b32 s2, v253, 12
	v_readlane_b32 s3, v253, 13
	s_waitcnt vmcnt(0)
	s_nop 2
	global_atomic_add v207, v245, s[2:3]
	s_waitcnt vmcnt(0)

; __device__ __forceinline__ unsigned xb_ld(unsigned* p)              { return __hip_atomic_load(p, __ATOMIC_RELAXED, __HIP_MEMORY_SCOPE_AGENT); }
; __device__ __forceinline__ unsigned xb_add(unsigned* p, unsigned v) { return __hip_atomic_fetch_add(p, v, __ATOMIC_RELAXED, __HIP_MEMORY_SCOPE_AGENT); }
; #define XB_SPIN(cond, bar) do { unsigned _sp = 0; while (cond) { __builtin_amdgcn_s_sleep(1); \
;     if ((++_sp & 255u) == 0u) { if (xb_ld(&(bar)[XB_TMO])) break; if (_sp > XB_SPIN_CAP) { atomicAdd(&(bar)[XB_TMO], 1u); break; } } } } while (0)
; __device__ __forceinline__ void xcd_barrier(const XcdBarrier& b) {
;     ...
;         const unsigned old = xb_add(&bar[XB_XSUB(b.x)], 1u);
;         const unsigned gen = old / nloc;
;         if (old + 1u == (gen + 1u) * nloc) {
;             __builtin_amdgcn_fence(__ATOMIC_RELEASE, "agent");
;             asm volatile("s_waitcnt vmcnt(0)" ::: "memory");
;             const unsigned og = xb_add(&bar[XB_TOP], 1u);
;             const unsigned tg = og / nx;
;             if (og + 1u == (tg + 1u) * nx) xb_add(&bar[XB_TOPGEN], 1u);
;             else XB_SPIN(xb_ld(&bar[XB_TOPGEN]) == tg, bar);
;             __builtin_amdgcn_fence(__ATOMIC_ACQUIRE, "agent");
;             xb_add(&bar[XB_XGEN(b.x)], 1u);
;             asm volatile("s_waitcnt vmcnt(0)" ::: "memory");
;         } else {
;             XB_SPIN(xb_ld(&bar[XB_XGEN(b.x)]) == gen, bar);
.LBB0_430:
	v_readlane_b32 s2, v253, 10
	v_readlane_b32 s3, v253, 11
	v_cvt_f32_u32_e32 v3, v4
	v_sub_u32_e32 v6, 0, v4
	v_rcp_iflag_f32_e32 v3, v3
	s_nop 1
	global_atomic_add v5, v207, v245, s[2:3] sc0
	buffer_inv sc1
	v_mul_f32_e32 v3, 0x4f7ffffe, v3
	v_cvt_u32_f32_e32 v3, v3
	v_mul_lo_u32 v6, v6, v3
	v_mul_hi_u32 v6, v3, v6
	v_add_u32_e32 v3, v3, v6
	s_waitcnt vmcnt(1)
	v_mul_hi_u32 v3, v5, v3
	v_mul_lo_u32 v6, v3, v4
	v_sub_u32_e32 v6, v5, v6
	v_add_u32_e32 v7, 1, v3
	v_cmp_ge_u32_e32 vcc, v6, v4
	v_add_u32_e32 v5, 1, v5
	s_nop 0
	v_cndmask_b32_e32 v3, v3, v7, vcc
	v_sub_u32_e32 v7, v6, v4
	v_cndmask_b32_e32 v6, v6, v7, vcc
	v_add_u32_e32 v7, 1, v3
	v_cmp_ge_u32_e32 vcc, v6, v4
	s_nop 1
	v_cndmask_b32_e32 v3, v3, v7, vcc
	v_mul_lo_u32 v6, v4, v3
	v_add_u32_e32 v4, v6, v4
	v_cmp_ne_u32_e32 vcc, v5, v4
	s_and_saveexec_b64 s[2:3], vcc
	s_xor_b64 s[2:3], exec, s[2:3]
	s_cbranch_execz .LBB0_444
	v_readlane_b32 s12, v253, 12
	v_readlane_b32 s13, v253, 13
	s_waitcnt lgkmcnt(0)
	s_nop 3
	global_load_dword v2, v207, s[12:13] sc1
	s_waitcnt vmcnt(0)
	v_cmp_eq_u32_e32 vcc, v2, v3
	s_and_saveexec_b64 s[24:25], vcc
	s_cbranch_execz .LBB0_443
	s_mov_b32 s14, 1
	s_mov_b64 s[30:31], 0
	s_branch .LBB0_434

; __device__ __forceinline__ unsigned xb_ld(unsigned* p)              { return __hip_atomic_load(p, __ATOMIC_RELAXED, __HIP_MEMORY_SCOPE_AGENT); }
; #define XB_SPIN(cond, bar) do { unsigned _sp = 0; while (cond) { __builtin_amdgcn_s_sleep(1); \
;     if ((++_sp & 255u) == 0u) { if (xb_ld(&(bar)[XB_TMO])) break; if (_sp > XB_SPIN_CAP) { atomicAdd(&(bar)[XB_TMO], 1u); break; } } } } while (0)
; __device__ __forceinline__ void xcd_barrier(const XcdBarrier& b) {
;     ...
;             XB_SPIN(xb_ld(&bar[XB_XGEN(b.x)]) == gen, bar);
;             __builtin_amdgcn_fence(__ATOMIC_ACQUIRE, "agent");
;             asm volatile("s_waitcnt vmcnt(0)" ::: "memory");
.LBB0_443:
	s_or_b64 exec, exec, s[24:25]
	s_waitcnt vmcnt(0)
	s_waitcnt vmcnt(0)

; __device__ __forceinline__ unsigned xb_ld(unsigned* p)              { return __hip_atomic_load(p, __ATOMIC_RELAXED, __HIP_MEMORY_SCOPE_AGENT); }
; __device__ __forceinline__ unsigned xb_add(unsigned* p, unsigned v) { return __hip_atomic_fetch_add(p, v, __ATOMIC_RELAXED, __HIP_MEMORY_SCOPE_AGENT); }
; #define XB_SPIN(cond, bar) do { unsigned _sp = 0; while (cond) { __builtin_amdgcn_s_sleep(1); \
;     if ((++_sp & 255u) == 0u) { if (xb_ld(&(bar)[XB_TMO])) break; if (_sp > XB_SPIN_CAP) { atomicAdd(&(bar)[XB_TMO], 1u); break; } } } } while (0)
; __device__ __forceinline__ void xcd_barrier(const XcdBarrier& b) {
;     ...
;         const unsigned old = xb_add(&bar[XB_XSUB(b.x)], 1u);
;         const unsigned gen = old / nloc;
;         if (old + 1u == (gen + 1u) * nloc) {
;             __builtin_amdgcn_fence(__ATOMIC_RELEASE, "agent");
;             asm volatile("s_waitcnt vmcnt(0)" ::: "memory");
;             const unsigned og = xb_add(&bar[XB_TOP], 1u);
;             const unsigned tg = og / nx;
;             if (og + 1u == (tg + 1u) * nx) xb_add(&bar[XB_TOPGEN], 1u);
;             else XB_SPIN(xb_ld(&bar[XB_TOPGEN]) == tg, bar);
;             __builtin_amdgcn_fence(__ATOMIC_ACQUIRE, "agent");
;             xb_add(&bar[XB_XGEN(b.x)], 1u);
;             asm volatile("s_waitcnt vmcnt(0)" ::: "memory");
;         } else {
;             XB_SPIN(xb_ld(&bar[XB_XGEN(b.x)]) == gen, bar);
.LBB0_1358:
	v_readlane_b32 s12, v253, 10
	v_readlane_b32 s13, v253, 11
	v_cvt_f32_u32_e32 v3, v4
	v_sub_u32_e32 v6, 0, v4
	v_rcp_iflag_f32_e32 v3, v3
	s_nop 1
	global_atomic_add v5, v207, v245, s[12:13] sc0
	buffer_inv sc1
	v_mul_f32_e32 v3, 0x4f7ffffe, v3
	v_cvt_u32_f32_e32 v3, v3
	v_mul_lo_u32 v6, v6, v3
	v_mul_hi_u32 v6, v3, v6
	v_add_u32_e32 v3, v3, v6
	s_waitcnt vmcnt(1)
	v_mul_hi_u32 v3, v5, v3
	v_mul_lo_u32 v6, v3, v4
	v_sub_u32_e32 v6, v5, v6
	v_add_u32_e32 v7, 1, v3
	v_cmp_ge_u32_e32 vcc, v6, v4
	v_add_u32_e32 v5, 1, v5
	s_nop 0
	v_cndmask_b32_e32 v3, v3, v7, vcc
	v_sub_u32_e32 v7, v6, v4
	v_cndmask_b32_e32 v6, v6, v7, vcc
	v_add_u32_e32 v7, 1, v3
	v_cmp_ge_u32_e32 vcc, v6, v4
	s_nop 1
	v_cndmask_b32_e32 v3, v3, v7, vcc
	v_mul_lo_u32 v6, v4, v3
	v_add_u32_e32 v4, v6, v4
	v_cmp_ne_u32_e32 vcc, v5, v4
	s_and_saveexec_b64 s[12:13], vcc
	s_xor_b64 s[24:25], exec, s[12:13]
	s_cbranch_execz .LBB0_1372
	v_readlane_b32 s12, v253, 12
	v_readlane_b32 s13, v253, 13
	s_waitcnt lgkmcnt(0)
	s_nop 3
	global_load_dword v2, v207, s[12:13] sc1
	s_waitcnt vmcnt(0)
	v_cmp_eq_u32_e32 vcc, v2, v3
	s_and_saveexec_b64 s[30:31], vcc
	s_cbranch_execz .LBB0_1371
	s_mov_b32 s14, 1
	s_mov_b64 s[36:37], 0
	s_branch .LBB0_1362

; __device__ __forceinline__ unsigned xb_ld(unsigned* p)              { return __hip_atomic_load(p, __ATOMIC_RELAXED, __HIP_MEMORY_SCOPE_AGENT); }
; #define XB_SPIN(cond, bar) do { unsigned _sp = 0; while (cond) { __builtin_amdgcn_s_sleep(1); \
;     if ((++_sp & 255u) == 0u) { if (xb_ld(&(bar)[XB_TMO])) break; if (_sp > XB_SPIN_CAP) { atomicAdd(&(bar)[XB_TMO], 1u); break; } } } } while (0)
; __device__ __forceinline__ void xcd_barrier(const XcdBarrier& b) {
;     ...
;             XB_SPIN(xb_ld(&bar[XB_XGEN(b.x)]) == gen, bar);
;             __builtin_amdgcn_fence(__ATOMIC_ACQUIRE, "agent");
;             asm volatile("s_waitcnt vmcnt(0)" ::: "memory");
.LBB0_1371:
	s_or_b64 exec, exec, s[30:31]
	s_waitcnt vmcnt(0)
	s_waitcnt vmcnt(0)

; __device__ __forceinline__ unsigned xb_add(unsigned* p, unsigned v) { return __hip_atomic_fetch_add(p, v, __ATOMIC_RELAXED, __HIP_MEMORY_SCOPE_AGENT); }
; __device__ __forceinline__ void xcd_barrier(const XcdBarrier& b) {
;     ...
;             __builtin_amdgcn_fence(__ATOMIC_ACQUIRE, "agent");
;             xb_add(&bar[XB_XGEN(b.x)], 1u);
;             asm volatile("s_waitcnt vmcnt(0)" ::: "memory");
.LBB0_1389:
	s_or_b64 exec, exec, s[24:25]
	v_readlane_b32 s12, v253, 12
	v_readlane_b32 s13, v253, 13
	s_waitcnt vmcnt(0)
	s_nop 2
	global_atomic_add v207, v245, s[12:13]
	s_waitcnt vmcnt(0)

; __device__ __forceinline__ unsigned xb_ld(unsigned* p)              { return __hip_atomic_load(p, __ATOMIC_RELAXED, __HIP_MEMORY_SCOPE_AGENT); }
; __device__ __forceinline__ unsigned xb_add(unsigned* p, unsigned v) { return __hip_atomic_fetch_add(p, v, __ATOMIC_RELAXED, __HIP_MEMORY_SCOPE_AGENT); }
; #define XB_SPIN(cond, bar) do { unsigned _sp = 0; while (cond) { __builtin_amdgcn_s_sleep(1); \
;     if ((++_sp & 255u) == 0u) { if (xb_ld(&(bar)[XB_TMO])) break; if (_sp > XB_SPIN_CAP) { atomicAdd(&(bar)[XB_TMO], 1u); break; } } } } while (0)
; __device__ __forceinline__ void xcd_barrier(const XcdBarrier& b) {
;     ...
;         const unsigned old = xb_add(&bar[XB_XSUB(b.x)], 1u);
;         const unsigned gen = old / nloc;
;         if (old + 1u == (gen + 1u) * nloc) {
;             __builtin_amdgcn_fence(__ATOMIC_RELEASE, "agent");
;             asm volatile("s_waitcnt vmcnt(0)" ::: "memory");
;             const unsigned og = xb_add(&bar[XB_TOP], 1u);
;             const unsigned tg = og / nx;
;             if (og + 1u == (tg + 1u) * nx) xb_add(&bar[XB_TOPGEN], 1u);
;             else XB_SPIN(xb_ld(&bar[XB_TOPGEN]) == tg, bar);
;             __builtin_amdgcn_fence(__ATOMIC_ACQUIRE, "agent");
;             xb_add(&bar[XB_XGEN(b.x)], 1u);
;             asm volatile("s_waitcnt vmcnt(0)" ::: "memory");
;         } else {
;             XB_SPIN(xb_ld(&bar[XB_XGEN(b.x)]) == gen, bar);
.LBB0_2710:
	v_readlane_b32 s2, v253, 10
	v_readlane_b32 s3, v253, 11
	v_cvt_f32_u32_e32 v3, v4
	v_sub_u32_e32 v6, 0, v4
	v_rcp_iflag_f32_e32 v3, v3
	s_nop 1
	global_atomic_add v5, v207, v245, s[2:3] sc0
	buffer_inv sc1
	v_mul_f32_e32 v3, 0x4f7ffffe, v3
	v_cvt_u32_f32_e32 v3, v3
	v_mul_lo_u32 v6, v6, v3
	v_mul_hi_u32 v6, v3, v6
	v_add_u32_e32 v3, v3, v6
	s_waitcnt vmcnt(1)
	v_mul_hi_u32 v3, v5, v3
	v_mul_lo_u32 v6, v3, v4
	v_sub_u32_e32 v6, v5, v6
	v_add_u32_e32 v7, 1, v3
	v_cmp_ge_u32_e32 vcc, v6, v4
	v_add_u32_e32 v5, 1, v5
	s_nop 0
	v_cndmask_b32_e32 v3, v3, v7, vcc
	v_sub_u32_e32 v7, v6, v4
	v_cndmask_b32_e32 v6, v6, v7, vcc
	v_add_u32_e32 v7, 1, v3
	v_cmp_ge_u32_e32 vcc, v6, v4
	s_nop 1
	v_cndmask_b32_e32 v3, v3, v7, vcc
	v_mul_lo_u32 v6, v4, v3
	v_add_u32_e32 v4, v6, v4
	v_cmp_ne_u32_e32 vcc, v5, v4
	s_and_saveexec_b64 s[2:3], vcc
	s_xor_b64 s[2:3], exec, s[2:3]
	s_cbranch_execz .LBB0_2724
	v_readlane_b32 s12, v253, 12
	v_readlane_b32 s13, v253, 13
	s_waitcnt lgkmcnt(0)
	s_nop 3
	global_load_dword v2, v207, s[12:13] sc1
	s_waitcnt vmcnt(0)
	v_cmp_eq_u32_e32 vcc, v2, v3
	s_and_saveexec_b64 s[24:25], vcc
	s_cbranch_execz .LBB0_2723
	s_mov_b32 s4, 1
	s_mov_b64 s[30:31], 0
	s_branch .LBB0_2714
